# speedup vs baseline: 1.0434x; 1.0434x over previous
.LBB0_11:
	s_add_i32 s3, s3, 2
	s_cmp_gt_u32 s3, 5
	s_cselect_b64 vcc, -1, 0
	v_add_u32_e32 v184, 0xffff0000, v183
	s_and_b64 s[12:13], vcc, exec
	v_cndmask_b32_e32 v200, v184, v1, vcc
	s_cselect_b32 s15, 0x20000, 0x20000
	s_cselect_b32 s14, 0x10000, s16
	s_cselect_b32 s13, s41, s37
	s_cselect_b32 s12, s22, s36
	s_waitcnt vmcnt(8)
	v_cvt_pk_f16_f32 v187, v172, v176
	v_cvt_pk_f16_f32 v186, v160, v168
	v_cvt_pk_f16_f32 v185, v164, v156
	v_cvt_pk_f16_f32 v184, v148, v152
	v_cvt_pk_f16_f32 v191, v173, v177
	v_cvt_pk_f16_f32 v190, v161, v169
	v_cvt_pk_f16_f32 v189, v165, v157
	v_cvt_pk_f16_f32 v188, v149, v153
	v_cvt_pk_f16_f32 v195, v174, v178
	v_cvt_pk_f16_f32 v194, v162, v170
	v_cvt_pk_f16_f32 v193, v166, v158
	v_cvt_pk_f16_f32 v192, v150, v154
	v_cvt_pk_f16_f32 v199, v175, v179
	v_cvt_pk_f16_f32 v198, v163, v171
	v_cvt_pk_f16_f32 v197, v167, v159
	v_cvt_pk_f16_f32 v196, v151, v155
	buffer_load_dwordx4 v[148:151], v200, s[12:15], 0 offen nt
	buffer_load_dwordx4 v[152:155], v200, s[12:15], 0 offen offset:512 nt
	buffer_load_dwordx4 v[164:167], v200, s[12:15], 0 offen offset:1024 nt
	buffer_load_dwordx4 v[156:159], v200, s[12:15], 0 offen offset:1536 nt
	buffer_load_dwordx4 v[160:163], v200, s[12:15], 0 offen offset:2048 nt
	buffer_load_dwordx4 v[168:171], v200, s[12:15], 0 offen offset:2560 nt
	buffer_load_dwordx4 v[172:175], v200, s[12:15], 0 offen offset:3072 nt
	buffer_load_dwordx4 v[176:179], v200, s[12:15], 0 offen offset:3584 nt
	ds_write_b128 v180, v[184:187]
	ds_write_b128 v180, v[188:191] offset:1024
	ds_write_b128 v180, v[192:195] offset:2048
	ds_write_b128 v180, v[196:199] offset:3072
	s_cselect_b32 s14, s17, 0x8000000
	s_cselect_b32 s13, s29, s37
	s_cselect_b32 s12, s28, s36
	v_cndmask_b32_e32 v200, v183, v1, vcc
	s_cmp_lg_u32 s3, 0
	s_cbranch_scc1 .Lw47_not0
	global_load_dwordx4 v[48:51], v247, s[68:69]
	global_load_dwordx4 v[80:83], v247, s[44:45]
	v_add_u32_e32 v247, 0x2000, v247
	global_load_dwordx4 v[52:55], v247, s[68:69]
	global_load_dwordx4 v[84:87], v247, s[44:45]
	v_add_u32_e32 v247, 0x2000, v247
	global_load_dwordx4 v[56:59], v247, s[68:69]
	global_load_dwordx4 v[88:91], v247, s[44:45]
	v_add_u32_e32 v247, 0x2000, v247
	global_load_dwordx4 v[60:63], v247, s[68:69]
	global_load_dwordx4 v[92:95], v247, s[44:45]
	v_add_u32_e32 v247, 0x2000, v247
	s_branch .Lw47_xdone
.Lw47_not0:
	s_cmp_lg_u32 s3, 2
	s_cbranch_scc1 .Lw47_not2
	global_load_dwordx4 v[64:67], v247, s[68:69]
	global_load_dwordx4 v[96:99], v247, s[44:45]
	v_add_u32_e32 v247, 0x2000, v247
	global_load_dwordx4 v[68:71], v247, s[68:69]
	global_load_dwordx4 v[100:103], v247, s[44:45]
	v_add_u32_e32 v247, 0x2000, v247
	global_load_dwordx4 v[72:75], v247, s[68:69]
	global_load_dwordx4 v[104:107], v247, s[44:45]
	v_add_u32_e32 v247, 0x2000, v247
	global_load_dwordx4 v[76:79], v247, s[68:69]
	global_load_dwordx4 v[108:111], v247, s[44:45]
	s_branch .Lw47_xdone
.Lw47_not2:
	s_cmp_lg_u32 s3, 4
	s_cbranch_scc1 .Lw47_xdone
	v_cvt_pk_f16_f32 v48, v48, v49
	v_cvt_pk_f16_f32 v49, v50, v51
	ds_write_b64 v246, v[48:49]
	v_cvt_pk_f16_f32 v80, v80, v81
	v_cvt_pk_f16_f32 v81, v82, v83
	ds_write_b64 v246, v[80:81] offset:34816
	v_cvt_pk_f16_f32 v52, v52, v53
	v_cvt_pk_f16_f32 v53, v54, v55
	ds_write_b64 v246, v[52:53] offset:4352
	v_cvt_pk_f16_f32 v84, v84, v85
	v_cvt_pk_f16_f32 v85, v86, v87
	ds_write_b64 v246, v[84:85] offset:39168
	v_cvt_pk_f16_f32 v56, v56, v57
	v_cvt_pk_f16_f32 v57, v58, v59
	ds_write_b64 v246, v[56:57] offset:8704
	v_cvt_pk_f16_f32 v88, v88, v89
	v_cvt_pk_f16_f32 v89, v90, v91
	ds_write_b64 v246, v[88:89] offset:43520
	v_cvt_pk_f16_f32 v60, v60, v61
	v_cvt_pk_f16_f32 v61, v62, v63
	ds_write_b64 v246, v[60:61] offset:13056
	v_cvt_pk_f16_f32 v92, v92, v93
	v_cvt_pk_f16_f32 v93, v94, v95
	ds_write_b64 v246, v[92:93] offset:47872
	v_cvt_pk_f16_f32 v64, v64, v65
	v_cvt_pk_f16_f32 v65, v66, v67
	ds_write_b64 v246, v[64:65] offset:17408
	v_cvt_pk_f16_f32 v96, v96, v97
	v_cvt_pk_f16_f32 v97, v98, v99
	ds_write_b64 v246, v[96:97] offset:52224
	v_cvt_pk_f16_f32 v68, v68, v69
	v_cvt_pk_f16_f32 v69, v70, v71
	ds_write_b64 v246, v[68:69] offset:21760
	v_cvt_pk_f16_f32 v100, v100, v101
	v_cvt_pk_f16_f32 v101, v102, v103
	ds_write_b64 v246, v[100:101] offset:56576
	v_cvt_pk_f16_f32 v72, v72, v73
	v_cvt_pk_f16_f32 v73, v74, v75
	ds_write_b64 v246, v[72:73] offset:26112
	v_cvt_pk_f16_f32 v104, v104, v105
	v_cvt_pk_f16_f32 v105, v106, v107
	ds_write_b64 v246, v[104:105] offset:60928
	v_cvt_pk_f16_f32 v76, v76, v77
	v_cvt_pk_f16_f32 v77, v78, v79
	ds_write_b64 v246, v[76:77] offset:30464
	v_cvt_pk_f16_f32 v108, v108, v109
	v_cvt_pk_f16_f32 v109, v110, v111
	ds_write_b64 v246, v[108:109] offset:65280
.Lw47_xdone:
	s_waitcnt lgkmcnt(0)
	s_barrier
	s_cmp_lg_u32 s3, 4
	s_cbranch_scc1 .Lw47_ydone
	ds_read_b128 v[92:95], v248
	ds_read_b128 v[88:91], v248 offset:32
	ds_read_b128 v[84:87], v248 offset:64
	ds_read_b128 v[80:83], v248 offset:96
	ds_read_b128 v[76:79], v248 offset:128
	ds_read_b128 v[72:75], v248 offset:160
	ds_read_b128 v[68:71], v248 offset:192
	ds_read_b128 v[64:67], v248 offset:224
	ds_read2_b64 v[60:63], v249 offset1:2
	ds_read2_b64 v[56:59], v249 offset0:4 offset1:6
	ds_read2_b64 v[52:55], v249 offset0:8 offset1:10
	ds_read2_b64 v[48:51], v249 offset0:12 offset1:14
	s_waitcnt lgkmcnt(0)
.Lw47_ydone:
	ds_read_b128 v[184:187], v181
	ds_read_b128 v[188:191], v182
	ds_read_b128 v[192:195], v182 offset:1024
	ds_read_b128 v[196:199], v181 offset:4096
	s_waitcnt lgkmcnt(2)
	v_mfma_f32_32x32x16_f16 v[18:33], v[184:187], v[188:191], v[18:33]
	s_waitcnt lgkmcnt(1)
	v_mfma_f32_32x32x16_f16 v[2:17], v[184:187], v[192:195], v[2:17]
	ds_read_b128 v[184:187], v182 offset:4096
	ds_read_b128 v[188:191], v182 offset:5120
	s_waitcnt lgkmcnt(1)
	v_mfma_f32_32x32x16_f16 v[18:33], v[196:199], v[184:187], v[18:33]
	s_waitcnt lgkmcnt(0)
	v_mfma_f32_32x32x16_f16 v[2:17], v[196:199], v[188:191], v[2:17]
	ds_read_b128 v[184:187], v181 offset:8192
	ds_read_b128 v[188:191], v182 offset:8192
	ds_read_b128 v[192:195], v182 offset:9216
	ds_read_b128 v[196:199], v181 offset:12288
	s_waitcnt lgkmcnt(2)
	v_mfma_f32_32x32x16_f16 v[18:33], v[184:187], v[188:191], v[18:33]
	s_waitcnt lgkmcnt(1)
	v_mfma_f32_32x32x16_f16 v[2:17], v[184:187], v[192:195], v[2:17]
	ds_read_b128 v[184:187], v182 offset:12288
	ds_read_b128 v[188:191], v182 offset:13312
	s_waitcnt lgkmcnt(1)
	v_mfma_f32_32x32x16_f16 v[18:33], v[196:199], v[184:187], v[18:33]
	s_waitcnt lgkmcnt(0)
	v_mfma_f32_32x32x16_f16 v[2:17], v[196:199], v[188:191], v[2:17]
	ds_read_b128 v[184:187], v181 offset:16384
	ds_read_b128 v[188:191], v182 offset:16384
	ds_read_b128 v[192:195], v182 offset:17408
	ds_read_b128 v[196:199], v181 offset:20480
	s_waitcnt lgkmcnt(2)
	v_mfma_f32_32x32x16_f16 v[18:33], v[184:187], v[188:191], v[18:33]
	s_waitcnt lgkmcnt(1)
	v_mfma_f32_32x32x16_f16 v[2:17], v[184:187], v[192:195], v[2:17]
	ds_read_b128 v[184:187], v182 offset:20480
	ds_read_b128 v[188:191], v182 offset:21504
	s_waitcnt lgkmcnt(1)
	v_mfma_f32_32x32x16_f16 v[18:33], v[196:199], v[184:187], v[18:33]
	s_waitcnt lgkmcnt(0)
	v_mfma_f32_32x32x16_f16 v[2:17], v[196:199], v[188:191], v[2:17]
	ds_read_b128 v[184:187], v181 offset:24576
	ds_read_b128 v[188:191], v182 offset:24576
	ds_read_b128 v[192:195], v182 offset:25600
	ds_read_b128 v[196:199], v181 offset:28672
	s_waitcnt lgkmcnt(2)
	v_mfma_f32_32x32x16_f16 v[18:33], v[184:187], v[188:191], v[18:33]
	s_waitcnt lgkmcnt(1)
	v_mfma_f32_32x32x16_f16 v[2:17], v[184:187], v[192:195], v[2:17]
	ds_read_b128 v[184:187], v182 offset:28672
	ds_read_b128 v[188:191], v182 offset:29696
	s_waitcnt lgkmcnt(1)
	v_mfma_f32_32x32x16_f16 v[18:33], v[196:199], v[184:187], v[18:33]
	s_waitcnt lgkmcnt(0)
	v_mfma_f32_32x32x16_f16 v[2:17], v[196:199], v[188:191], v[2:17]
	s_cmp_gt_u32 s3, 2
	s_cbranch_scc1 .Lw47_w8
	s_waitcnt vmcnt(16)
	s_branch .Lw47_wdone

.LBB0_13:
	s_or_saveexec_b64 s[10:11], s[10:11]
	v_mov_b32_e32 v217, 0
	s_xor_b64 exec, exec, s[10:11]
	s_cbranch_execz .LBB0_19
	s_nop 6
	v_add_u32_e32 v2, 0x20000, v180
	buffer_load_dwordx4 v[148:151], v2, s[36:39], 0 offen nt
	buffer_load_dwordx4 v[152:155], v2, s[36:39], 0 offen offset:512 nt
	buffer_load_dwordx4 v[164:167], v2, s[36:39], 0 offen offset:1024 nt
	buffer_load_dwordx4 v[156:159], v2, s[36:39], 0 offen offset:1536 nt
	buffer_load_dwordx4 v[160:163], v2, s[36:39], 0 offen offset:2048 nt
	buffer_load_dwordx4 v[168:171], v2, s[36:39], 0 offen offset:2560 nt
	buffer_load_dwordx4 v[172:175], v2, s[36:39], 0 offen offset:3072 nt
	buffer_load_dwordx4 v[176:179], v2, s[36:39], 0 offen offset:3584 nt
	v_lshlrev_b32_e32 v233, 4, v218
	s_waitcnt vmcnt(16)
	v_cvt_pk_f16_f32 v5, v108, v112
	v_cvt_pk_f16_f32 v4, v100, v104
	v_cvt_pk_f16_f32 v3, v42, v96
	v_cvt_pk_f16_f32 v2, v34, v38
	v_lshl_or_b32 v234, v219, 12, v233
	ds_write_b128 v234, v[2:5]
	v_cvt_pk_f16_f32 v5, v109, v113
	v_cvt_pk_f16_f32 v4, v101, v105
	v_cvt_pk_f16_f32 v3, v43, v97
	v_cvt_pk_f16_f32 v2, v35, v39
	ds_write_b128 v234, v[2:5] offset:1024
	v_cvt_pk_f16_f32 v5, v110, v114
	v_cvt_pk_f16_f32 v4, v102, v106
	v_cvt_pk_f16_f32 v3, v44, v98
	v_cvt_pk_f16_f32 v2, v36, v40
	s_movk_i32 s12, 0xf400
	ds_write_b128 v234, v[2:5] offset:2048
	v_cvt_pk_f16_f32 v5, v111, v115
	v_cvt_pk_f16_f32 v4, v103, v107
	v_cvt_pk_f16_f32 v3, v45, v99
	v_cvt_pk_f16_f32 v2, v37, v41
	v_mad_i32_i24 v235, v219, s12, v234
	s_add_i32 s12, s46, s33
	ds_write_b128 v234, v[2:5] offset:3072
	global_load_dwordx4 v[48:51], v247, s[68:69]
	global_load_dwordx4 v[80:83], v247, s[44:45]
	v_add_u32_e32 v247, 0x2000, v247
	global_load_dwordx4 v[52:55], v247, s[68:69]
	global_load_dwordx4 v[84:87], v247, s[44:45]
	v_add_u32_e32 v247, 0x2000, v247
	global_load_dwordx4 v[56:59], v247, s[68:69]
	global_load_dwordx4 v[88:91], v247, s[44:45]
	v_add_u32_e32 v247, 0x2000, v247
	global_load_dwordx4 v[60:63], v247, s[68:69]
	global_load_dwordx4 v[92:95], v247, s[44:45]
	v_add_u32_e32 v247, 0x2000, v247
	v_add3_u32 v2, s12, v216, v221
	v_lshl_or_b32 v2, v2, 9, v232
	v_mov_b32_e32 v217, 0
	s_mov_b32 s3, 0
	v_add_u32_e32 v236, 0x40000, v2
	s_mov_b32 s16, 0x10000
	v_mov_b32_e32 v2, v217
	v_mov_b32_e32 v3, v217
	v_mov_b32_e32 v4, v217
	v_mov_b32_e32 v5, v217
	v_mov_b32_e32 v6, v217
	v_mov_b32_e32 v7, v217
	v_mov_b32_e32 v8, v217
	v_mov_b32_e32 v9, v217
	v_mov_b32_e32 v10, v217
	v_mov_b32_e32 v11, v217
	v_mov_b32_e32 v12, v217
	v_mov_b32_e32 v13, v217
	v_mov_b32_e32 v14, v217
	v_mov_b32_e32 v15, v217
	v_mov_b32_e32 v16, v217
	v_mov_b32_e32 v17, v217
	v_mov_b32_e32 v18, v217
	v_mov_b32_e32 v19, v217
	v_mov_b32_e32 v20, v217
	v_mov_b32_e32 v21, v217
	v_mov_b32_e32 v22, v217
	v_mov_b32_e32 v23, v217
	v_mov_b32_e32 v24, v217
	v_mov_b32_e32 v25, v217
	v_mov_b32_e32 v26, v217
	v_mov_b32_e32 v27, v217
	v_mov_b32_e32 v28, v217
	v_mov_b32_e32 v29, v217
	v_mov_b32_e32 v30, v217
	v_mov_b32_e32 v31, v217
	v_mov_b32_e32 v32, v217
	v_mov_b32_e32 v33, v217
	s_branch .LBB0_16
.LBB0_15:
	s_cmp_gt_u32 s3, 3
	s_cselect_b64 vcc, -1, 0
	s_and_b64 s[14:15], vcc, exec
	s_waitcnt vmcnt(8)
	v_cndmask_b32_e32 v176, v236, v1, vcc
	s_cselect_b32 s55, 0x20000, 0x20000
	s_cselect_b32 s54, s16, 0x8000000
	s_cselect_b32 s53, s41, s37
	s_cselect_b32 s52, s22, s36
	buffer_load_dwordx4 v[148:151], v176, s[52:55], 0 offen nt
	buffer_load_dwordx4 v[152:155], v176, s[52:55], 0 offen offset:512 nt
	buffer_load_dwordx4 v[164:167], v176, s[52:55], 0 offen offset:1024 nt
	buffer_load_dwordx4 v[156:159], v176, s[52:55], 0 offen offset:1536 nt
	buffer_load_dwordx4 v[160:163], v176, s[52:55], 0 offen offset:2048 nt
	buffer_load_dwordx4 v[168:171], v176, s[52:55], 0 offen offset:2560 nt
	buffer_load_dwordx4 v[172:175], v176, s[52:55], 0 offen offset:3072 nt
	s_nop 0
	buffer_load_dwordx4 v[176:179], v176, s[52:55], 0 offen offset:3584 nt
	s_cmp_lg_u32 s3, 0
	s_cbranch_scc1 .Lw03_nob
	global_load_dwordx4 v[64:67], v247, s[68:69]
	global_load_dwordx4 v[96:99], v247, s[44:45]
	v_add_u32_e32 v247, 0x2000, v247
	global_load_dwordx4 v[68:71], v247, s[68:69]
	global_load_dwordx4 v[100:103], v247, s[44:45]
	v_add_u32_e32 v247, 0x2000, v247
	global_load_dwordx4 v[72:75], v247, s[68:69]
	global_load_dwordx4 v[104:107], v247, s[44:45]
	v_add_u32_e32 v247, 0x2000, v247
	global_load_dwordx4 v[76:79], v247, s[68:69]
	global_load_dwordx4 v[108:111], v247, s[44:45]
.Lw03_nob:
	v_dot2c_f32_f16_e32 v217, 0x3c003c00, v180
	v_dot2c_f32_f16_e32 v217, 0x3c003c00, v181
	v_dot2c_f32_f16_e32 v217, 0x3c003c00, v182
	v_dot2c_f32_f16_e32 v217, 0x3c003c00, v183
	v_dot2c_f32_f16_e32 v217, 0x3c003c00, v184
	v_dot2c_f32_f16_e32 v217, 0x3c003c00, v185
	v_dot2c_f32_f16_e32 v217, 0x3c003c00, v186
	v_dot2c_f32_f16_e32 v217, 0x3c003c00, v187
	v_dot2c_f32_f16_e32 v217, 0x3c003c00, v188
	v_dot2c_f32_f16_e32 v217, 0x3c003c00, v189
	v_dot2c_f32_f16_e32 v217, 0x3c003c00, v190
	v_dot2c_f32_f16_e32 v217, 0x3c003c00, v191
	v_dot2c_f32_f16_e32 v217, 0x3c003c00, v192
	v_dot2c_f32_f16_e32 v217, 0x3c003c00, v193
	v_dot2c_f32_f16_e32 v217, 0x3c003c00, v194
	v_dot2c_f32_f16_e32 v217, 0x3c003c00, v195
	v_dot2c_f32_f16_e32 v217, 0x3c003c00, v196
	v_dot2c_f32_f16_e32 v217, 0x3c003c00, v197
	v_dot2c_f32_f16_e32 v217, 0x3c003c00, v198
	v_dot2c_f32_f16_e32 v217, 0x3c003c00, v199
	v_dot2c_f32_f16_e32 v217, 0x3c003c00, v200
	v_dot2c_f32_f16_e32 v217, 0x3c003c00, v201
	v_dot2c_f32_f16_e32 v217, 0x3c003c00, v202
	v_dot2c_f32_f16_e32 v217, 0x3c003c00, v203
	v_dot2c_f32_f16_e32 v217, 0x3c003c00, v204
	v_dot2c_f32_f16_e32 v217, 0x3c003c00, v205
	v_dot2c_f32_f16_e32 v217, 0x3c003c00, v206
	v_dot2c_f32_f16_e32 v217, 0x3c003c00, v207
	v_dot2c_f32_f16_e32 v217, 0x3c003c00, v208
	v_dot2c_f32_f16_e32 v217, 0x3c003c00, v209
	v_dot2c_f32_f16_e32 v217, 0x3c003c00, v210
	v_dot2c_f32_f16_e32 v217, 0x3c003c00, v211
	s_add_i32 s3, s3, 2
	ds_read_b128 v[180:183], v235 offset:32768
	ds_read_b128 v[184:187], v233 offset:32768
	ds_read_b128 v[188:191], v233 offset:33792
	ds_read_b128 v[192:195], v235 offset:36864
	v_add_u32_e32 v236, 0x20000, v236
	s_waitcnt lgkmcnt(3)
	v_dot2c_f32_f16_e32 v217, 0x3c003c00, v180
	s_waitcnt lgkmcnt(2)
	v_mfma_f32_32x32x16_f16 v[18:33], v[180:183], v[184:187], v[18:33]
	v_dot2c_f32_f16_e32 v217, 0x3c003c00, v181
	v_dot2c_f32_f16_e32 v217, 0x3c003c00, v182
	v_dot2c_f32_f16_e32 v217, 0x3c003c00, v183
	s_waitcnt lgkmcnt(0)
	v_dot2c_f32_f16_e32 v217, 0x3c003c00, v192
	v_dot2c_f32_f16_e32 v217, 0x3c003c00, v193
	v_dot2c_f32_f16_e32 v217, 0x3c003c00, v194
	v_dot2c_f32_f16_e32 v217, 0x3c003c00, v195
	v_mfma_f32_32x32x16_f16 v[2:17], v[180:183], v[188:191], v[2:17]
	ds_read_b128 v[184:187], v233 offset:36864
	ds_read_b128 v[188:191], v233 offset:37888
	s_and_b64 vcc, exec, s[12:13]
	s_waitcnt lgkmcnt(1)
	v_mfma_f32_32x32x16_f16 v[18:33], v[192:195], v[184:187], v[18:33]
	s_waitcnt lgkmcnt(0)
	v_mfma_f32_32x32x16_f16 v[2:17], v[192:195], v[188:191], v[2:17]
	ds_read_b128 v[184:187], v235 offset:40960
	ds_read_b128 v[188:191], v233 offset:40960
	ds_read_b128 v[196:199], v233 offset:41984
	ds_read_b128 v[200:203], v235 offset:45056
	s_waitcnt lgkmcnt(3)
	v_dot2c_f32_f16_e32 v217, 0x3c003c00, v184
	v_dot2c_f32_f16_e32 v217, 0x3c003c00, v185
	v_dot2c_f32_f16_e32 v217, 0x3c003c00, v186
	v_dot2c_f32_f16_e32 v217, 0x3c003c00, v187
	s_waitcnt lgkmcnt(0)
	v_dot2c_f32_f16_e32 v217, 0x3c003c00, v200
	v_mfma_f32_32x32x16_f16 v[18:33], v[184:187], v[188:191], v[18:33]
	v_dot2c_f32_f16_e32 v217, 0x3c003c00, v201
	v_dot2c_f32_f16_e32 v217, 0x3c003c00, v202
	v_dot2c_f32_f16_e32 v217, 0x3c003c00, v203
	v_mfma_f32_32x32x16_f16 v[2:17], v[184:187], v[196:199], v[2:17]
	ds_read_b128 v[188:191], v233 offset:45056
	ds_read_b128 v[196:199], v233 offset:46080
	s_waitcnt lgkmcnt(1)
	v_mfma_f32_32x32x16_f16 v[18:33], v[200:203], v[188:191], v[18:33]
	s_waitcnt lgkmcnt(0)
	v_mfma_f32_32x32x16_f16 v[2:17], v[200:203], v[196:199], v[2:17]
	ds_read_b128 v[188:191], v235 offset:49152
	ds_read_b128 v[196:199], v233 offset:49152
	ds_read_b128 v[204:207], v233 offset:50176
	ds_read_b128 v[208:211], v235 offset:53248
	ds_read_b128 v[180:183], v233 offset:54272
	ds_read_b128 v[192:195], v235 offset:57344
	s_waitcnt lgkmcnt(5)
	v_dot2c_f32_f16_e32 v217, 0x3c003c00, v188
	v_dot2c_f32_f16_e32 v217, 0x3c003c00, v189
	v_dot2c_f32_f16_e32 v217, 0x3c003c00, v190
	v_dot2c_f32_f16_e32 v217, 0x3c003c00, v191
	s_waitcnt lgkmcnt(4)
	v_mfma_f32_32x32x16_f16 v[18:33], v[188:191], v[196:199], v[18:33]
	ds_read_b128 v[196:199], v233 offset:53248
	s_waitcnt lgkmcnt(3)
	v_dot2c_f32_f16_e32 v217, 0x3c003c00, v208
	v_dot2c_f32_f16_e32 v217, 0x3c003c00, v209
	v_dot2c_f32_f16_e32 v217, 0x3c003c00, v210
	v_dot2c_f32_f16_e32 v217, 0x3c003c00, v211
	v_mfma_f32_32x32x16_f16 v[2:17], v[188:191], v[204:207], v[2:17]
	s_waitcnt lgkmcnt(0)
	v_mfma_f32_32x32x16_f16 v[18:33], v[208:211], v[196:199], v[18:33]
	v_mfma_f32_32x32x16_f16 v[2:17], v[208:211], v[180:183], v[2:17]
	ds_read_b128 v[180:183], v233 offset:57344
	ds_read_b128 v[184:187], v233 offset:58368
	ds_read_b128 v[196:199], v235 offset:61440
	v_dot2c_f32_f16_e32 v217, 0x3c003c00, v192
	v_dot2c_f32_f16_e32 v217, 0x3c003c00, v193
	v_dot2c_f32_f16_e32 v217, 0x3c003c00, v194
	v_dot2c_f32_f16_e32 v217, 0x3c003c00, v195
	s_waitcnt lgkmcnt(0)
	v_dot2c_f32_f16_e32 v217, 0x3c003c00, v196
	v_mfma_f32_32x32x16_f16 v[18:33], v[192:195], v[180:183], v[18:33]
	ds_read_b128 v[180:183], v233 offset:61440
	v_dot2c_f32_f16_e32 v217, 0x3c003c00, v197
	v_dot2c_f32_f16_e32 v217, 0x3c003c00, v198
	v_dot2c_f32_f16_e32 v217, 0x3c003c00, v199
	v_mfma_f32_32x32x16_f16 v[2:17], v[192:195], v[184:187], v[2:17]
	ds_read_b128 v[184:187], v233 offset:62464
	s_waitcnt lgkmcnt(1)
	v_mfma_f32_32x32x16_f16 v[18:33], v[196:199], v[180:183], v[18:33]
	s_waitcnt lgkmcnt(0)
	v_mfma_f32_32x32x16_f16 v[2:17], v[196:199], v[184:187], v[2:17]
	s_cbranch_vccnz .LBB0_19
.LBB0_16:
	s_cmp_gt_u32 s3, 4
	s_cselect_b64 vcc, -1, 0
	v_add_u32_e32 v180, 0xffff0000, v236
	s_and_b64 s[12:13], vcc, exec
	v_cndmask_b32_e32 v196, v180, v1, vcc
	s_cselect_b32 s13, s29, s37
	s_cselect_b32 s12, s28, s36
	s_cselect_b32 s15, 0x20000, 0x20000
	s_cselect_b32 s14, s16, 0x8000000
	s_waitcnt lgkmcnt(0)
	s_barrier
	s_cmp_lg_u32 s3, 4
	s_cbranch_scc1 .Lw03_ydone
	ds_read_b128 v[92:95], v248
	ds_read_b128 v[88:91], v248 offset:32
	ds_read_b128 v[84:87], v248 offset:64
	ds_read_b128 v[80:83], v248 offset:96
	ds_read_b128 v[76:79], v248 offset:128
	ds_read_b128 v[72:75], v248 offset:160
	ds_read_b128 v[68:71], v248 offset:192
	ds_read_b128 v[64:67], v248 offset:224
	ds_read2_b64 v[60:63], v249 offset1:2
	ds_read2_b64 v[56:59], v249 offset0:4 offset1:6
	ds_read2_b64 v[52:55], v249 offset0:8 offset1:10
	ds_read2_b64 v[48:51], v249 offset0:12 offset1:14
	s_waitcnt lgkmcnt(0)
.Lw03_ydone:
	s_cmp_gt_u32 s3, 2
	s_cbranch_scc1 .Lw03_w8
	s_waitcnt vmcnt(16)
	s_branch .Lw03_wdone

.Lw03_wdone:
	v_cvt_pk_f16_f32 v183, v140, v144
	v_cvt_pk_f16_f32 v182, v132, v136
	v_cvt_pk_f16_f32 v181, v124, v128
	v_cvt_pk_f16_f32 v180, v116, v120
	v_cvt_pk_f16_f32 v187, v141, v145
	v_cvt_pk_f16_f32 v186, v133, v137
	v_cvt_pk_f16_f32 v185, v125, v129
	v_cvt_pk_f16_f32 v184, v117, v121
	v_cvt_pk_f16_f32 v191, v142, v146
	v_cvt_pk_f16_f32 v190, v134, v138
	v_cvt_pk_f16_f32 v189, v126, v130
	v_cvt_pk_f16_f32 v188, v118, v122
	v_cvt_pk_f16_f32 v195, v143, v147
	v_cvt_pk_f16_f32 v194, v135, v139
	v_cvt_pk_f16_f32 v193, v127, v131
	v_cvt_pk_f16_f32 v192, v119, v123
	buffer_load_dwordx4 v[116:119], v196, s[12:15], 0 offen nt
	buffer_load_dwordx4 v[120:123], v196, s[12:15], 0 offen offset:512 nt
	buffer_load_dwordx4 v[124:127], v196, s[12:15], 0 offen offset:1024 nt
	buffer_load_dwordx4 v[128:131], v196, s[12:15], 0 offen offset:1536 nt
	buffer_load_dwordx4 v[132:135], v196, s[12:15], 0 offen offset:2048 nt
	buffer_load_dwordx4 v[136:139], v196, s[12:15], 0 offen offset:2560 nt
	buffer_load_dwordx4 v[140:143], v196, s[12:15], 0 offen offset:3072 nt
	buffer_load_dwordx4 v[144:147], v196, s[12:15], 0 offen offset:3584 nt
	ds_write_b128 v234, v[180:183] offset:32768
	ds_write_b128 v234, v[184:187] offset:33792
	ds_write_b128 v234, v[188:191] offset:34816
	ds_write_b128 v234, v[192:195] offset:35840
	ds_read_b128 v[180:183], v235
	ds_read_b128 v[188:191], v233
	ds_read_b128 v[192:195], v233 offset:1024
	ds_read_b128 v[184:187], v235 offset:4096
	s_waitcnt lgkmcnt(2)
	v_mfma_f32_32x32x16_f16 v[18:33], v[180:183], v[188:191], v[18:33]
	s_waitcnt lgkmcnt(1)
	v_mfma_f32_32x32x16_f16 v[2:17], v[180:183], v[192:195], v[2:17]
	ds_read_b128 v[188:191], v233 offset:4096
	ds_read_b128 v[192:195], v233 offset:5120
	s_waitcnt lgkmcnt(1)
	v_mfma_f32_32x32x16_f16 v[18:33], v[184:187], v[188:191], v[18:33]
	s_waitcnt lgkmcnt(0)
	v_mfma_f32_32x32x16_f16 v[2:17], v[184:187], v[192:195], v[2:17]
	ds_read_b128 v[188:191], v235 offset:8192
	ds_read_b128 v[196:199], v233 offset:8192
	ds_read_b128 v[200:203], v233 offset:9216
	ds_read_b128 v[192:195], v235 offset:12288
	s_waitcnt lgkmcnt(2)
	v_mfma_f32_32x32x16_f16 v[18:33], v[188:191], v[196:199], v[18:33]
	s_waitcnt lgkmcnt(1)
	v_mfma_f32_32x32x16_f16 v[2:17], v[188:191], v[200:203], v[2:17]
	ds_read_b128 v[196:199], v233 offset:12288
	ds_read_b128 v[200:203], v233 offset:13312
	s_waitcnt lgkmcnt(1)
	v_mfma_f32_32x32x16_f16 v[18:33], v[192:195], v[196:199], v[18:33]
	s_waitcnt lgkmcnt(0)
	v_mfma_f32_32x32x16_f16 v[2:17], v[192:195], v[200:203], v[2:17]
	ds_read_b128 v[196:199], v235 offset:16384
	ds_read_b128 v[204:207], v233 offset:16384
	ds_read_b128 v[208:211], v233 offset:17408
	ds_read_b128 v[200:203], v235 offset:20480
	s_waitcnt lgkmcnt(2)
	v_mfma_f32_32x32x16_f16 v[18:33], v[196:199], v[204:207], v[18:33]
	s_waitcnt lgkmcnt(1)
	v_mfma_f32_32x32x16_f16 v[2:17], v[196:199], v[208:211], v[2:17]
	ds_read_b128 v[204:207], v233 offset:20480
	ds_read_b128 v[208:211], v233 offset:21504
	s_waitcnt lgkmcnt(1)
	v_mfma_f32_32x32x16_f16 v[18:33], v[200:203], v[204:207], v[18:33]
	s_waitcnt lgkmcnt(0)
	v_mfma_f32_32x32x16_f16 v[2:17], v[200:203], v[208:211], v[2:17]
	ds_read_b128 v[204:207], v235 offset:24576
	ds_read_b128 v[238:241], v233 offset:24576
	ds_read_b128 v[242:245], v233 offset:25600
	ds_read_b128 v[208:211], v235 offset:28672
	s_waitcnt lgkmcnt(2)
	v_mfma_f32_32x32x16_f16 v[18:33], v[204:207], v[238:241], v[18:33]
	s_waitcnt lgkmcnt(1)
	v_mfma_f32_32x32x16_f16 v[2:17], v[204:207], v[242:245], v[2:17]
	ds_read_b128 v[238:241], v233 offset:28672
	ds_read_b128 v[242:245], v233 offset:29696
	s_waitcnt lgkmcnt(1)
	v_mfma_f32_32x32x16_f16 v[18:33], v[208:211], v[238:241], v[18:33]
	s_waitcnt lgkmcnt(0)
	v_mfma_f32_32x32x16_f16 v[2:17], v[208:211], v[242:245], v[2:17]
	s_cmp_gt_u32 s3, 5
	s_cselect_b64 s[12:13], -1, 0
	s_and_b64 vcc, exec, s[12:13]
	s_barrier
	s_cbranch_vccnz .LBB0_15
	s_waitcnt vmcnt(8)
	v_cvt_pk_f16_f32 v241, v172, v176
	v_cvt_pk_f16_f32 v240, v160, v168
	v_cvt_pk_f16_f32 v239, v164, v156
	v_cvt_pk_f16_f32 v238, v148, v152
	ds_write_b128 v234, v[238:241]
	v_cvt_pk_f16_f32 v241, v173, v177
	v_cvt_pk_f16_f32 v240, v161, v169
	v_cvt_pk_f16_f32 v239, v165, v157
	v_cvt_pk_f16_f32 v238, v149, v153
	ds_write_b128 v234, v[238:241] offset:1024
	v_cvt_pk_f16_f32 v241, v174, v178
	v_cvt_pk_f16_f32 v240, v162, v170
	v_cvt_pk_f16_f32 v239, v166, v158
	v_cvt_pk_f16_f32 v238, v150, v154
	v_cvt_pk_f16_f32 v161, v175, v179
	v_cvt_pk_f16_f32 v160, v163, v171
	v_cvt_pk_f16_f32 v159, v167, v159
	v_cvt_pk_f16_f32 v158, v151, v155
	ds_write_b128 v234, v[238:241] offset:2048
	ds_write_b128 v234, v[158:161] offset:3072
	s_cmp_lg_u32 s3, 2
	s_cbranch_scc1 .LBB0_15
	v_cvt_pk_f16_f32 v48, v48, v49
	v_cvt_pk_f16_f32 v49, v50, v51
	ds_write_b64 v246, v[48:49]
	v_cvt_pk_f16_f32 v80, v80, v81
	v_cvt_pk_f16_f32 v81, v82, v83
	ds_write_b64 v246, v[80:81] offset:34816
	v_cvt_pk_f16_f32 v52, v52, v53
	v_cvt_pk_f16_f32 v53, v54, v55
	ds_write_b64 v246, v[52:53] offset:4352
	v_cvt_pk_f16_f32 v84, v84, v85
	v_cvt_pk_f16_f32 v85, v86, v87
	ds_write_b64 v246, v[84:85] offset:39168
	v_cvt_pk_f16_f32 v56, v56, v57
	v_cvt_pk_f16_f32 v57, v58, v59
	ds_write_b64 v246, v[56:57] offset:8704
	v_cvt_pk_f16_f32 v88, v88, v89
	v_cvt_pk_f16_f32 v89, v90, v91
	ds_write_b64 v246, v[88:89] offset:43520
	v_cvt_pk_f16_f32 v60, v60, v61
	v_cvt_pk_f16_f32 v61, v62, v63
	ds_write_b64 v246, v[60:61] offset:13056
	v_cvt_pk_f16_f32 v92, v92, v93
	v_cvt_pk_f16_f32 v93, v94, v95
	ds_write_b64 v246, v[92:93] offset:47872
	v_cvt_pk_f16_f32 v64, v64, v65
	v_cvt_pk_f16_f32 v65, v66, v67
	ds_write_b64 v246, v[64:65] offset:17408
	v_cvt_pk_f16_f32 v96, v96, v97
	v_cvt_pk_f16_f32 v97, v98, v99
	ds_write_b64 v246, v[96:97] offset:52224
	v_cvt_pk_f16_f32 v68, v68, v69
	v_cvt_pk_f16_f32 v69, v70, v71
	ds_write_b64 v246, v[68:69] offset:21760
	v_cvt_pk_f16_f32 v100, v100, v101
	v_cvt_pk_f16_f32 v101, v102, v103
	ds_write_b64 v246, v[100:101] offset:56576
	v_cvt_pk_f16_f32 v72, v72, v73
	v_cvt_pk_f16_f32 v73, v74, v75
	ds_write_b64 v246, v[72:73] offset:26112
	v_cvt_pk_f16_f32 v104, v104, v105
	v_cvt_pk_f16_f32 v105, v106, v107
	ds_write_b64 v246, v[104:105] offset:60928
	v_cvt_pk_f16_f32 v76, v76, v77
	v_cvt_pk_f16_f32 v77, v78, v79
	ds_write_b64 v246, v[76:77] offset:30464
	v_cvt_pk_f16_f32 v108, v108, v109
	v_cvt_pk_f16_f32 v109, v110, v111
	ds_write_b64 v246, v[108:109] offset:65280
	s_branch .LBB0_15
